# baseline (speedup 1.0000x reference)
.LBB1_73:
	s_or_b64 exec, exec, s[0:1]
	s_movk_i32 s0, 0x60
	v_cmp_gt_i32_e64 s[0:1], s0, v107
	v_lshl_add_u32 v5, v14, 3, 0
	s_waitcnt lgkmcnt(0)
	s_barrier
	s_and_saveexec_b64 s[98:99], s[0:1]
	s_cbranch_execz .LBB1_195
	v_add_u32_e32 v2, 0x18000, v5
	ds_read2_b64 v[10:13], v2 offset1:96
	v_add_u32_e32 v2, 0x400, v2
	ds_read2_b64 v[14:17], v2 offset0:64 offset1:160
	v_readlane_b32 s4, v230, 2
	v_readlane_b32 s6, v230, 4
	s_waitcnt vmcnt(0) lgkmcnt(1)
	v_fmamk_f32 v10, v7, 0x80000000, v10
	v_fmac_f32_e32 v10, 0, v6
	v_fma_f32 v11, 0, v7, v11
	v_fmac_f32_e32 v11, 0, v6
	v_fmac_f32_e32 v13, v7, v10
	v_fma_f32 v12, -v7, v11, v12
	v_fmac_f32_e32 v13, v6, v11
	v_fmac_f32_e32 v12, v6, v10
	s_waitcnt lgkmcnt(0)
	v_fma_f32 v2, -v7, v13, v14
	v_fmac_f32_e32 v2, v6, v12
	v_fma_f32 v10, v7, v12, v15
	v_fmac_f32_e32 v10, v6, v13
	v_fmac_f32_e32 v17, v7, v2
	v_readlane_b32 s7, v230, 5
	v_fma_f32 v16, -v7, v10, v16
	v_fmac_f32_e32 v17, v6, v10
	v_mov_b64_e32 v[10:11], s[6:7]
	v_mad_i64_i32 v[10:11], s[0:1], v98, s62, v[10:11]
	v_lshlrev_b64 v[8:9], 3, v[8:9]
	v_fmac_f32_e32 v16, v6, v2
	v_and_b32_e32 v13, -16, v98
	v_lshl_add_u64 v[10:11], v[10:11], 0, v[8:9]
	v_lshl_add_u64 v[8:9], s[6:7], 0, v[8:9]
	global_store_dwordx2 v[10:11], v[16:17], off sc1
	v_subrev_u32_e32 v42, s6, v8
	v_mul_u32_u24_e32 v43, 0xc00, v13
	v_add_u32_e32 v42, v42, v43
	global_load_dwordx2 v[40:41], v42, s[6:7] sc1
	global_load_dwordx2 v[38:39], v42, s[6:7] offset:3072 sc1
	v_add_u32_e32 v43, 0x1800, v42
	global_load_dwordx2 v[36:37], v43, s[6:7] sc1
	global_load_dwordx2 v[34:35], v43, s[6:7] offset:3072 sc1
	v_add_u32_e32 v43, 0x3000, v42
	global_load_dwordx2 v[32:33], v43, s[6:7] sc1
	global_load_dwordx2 v[30:31], v43, s[6:7] offset:3072 sc1
	v_add_u32_e32 v43, 0x4800, v42
	global_load_dwordx2 v[28:29], v43, s[6:7] sc1
	global_load_dwordx2 v[26:27], v43, s[6:7] offset:3072 sc1
	v_add_u32_e32 v43, 0x6000, v42
	global_load_dwordx2 v[24:25], v43, s[6:7] sc1
	global_load_dwordx2 v[22:23], v43, s[6:7] offset:3072 sc1
	v_add_u32_e32 v43, 0x7800, v42
	global_load_dwordx2 v[20:21], v43, s[6:7] sc1
	global_load_dwordx2 v[18:19], v43, s[6:7] offset:3072 sc1
	v_add_u32_e32 v43, 0x9000, v42
	global_load_dwordx2 v[16:17], v43, s[6:7] sc1
	global_load_dwordx2 v[14:15], v43, s[6:7] offset:3072 sc1
	v_add_u32_e32 v43, 0xa800, v42
	global_load_dwordx2 v[10:11], v43, s[6:7] sc1
	v_cmp_ne_u32_e64 s[30:31], 0, v122
	v_cmp_lt_u32_e64 s[28:29], 1, v122
	v_cmp_lt_u32_e64 s[26:27], 2, v122
	v_cmp_lt_u32_e64 s[24:25], 4, v122
	v_cmp_lt_u32_e64 s[22:23], 5, v122
	v_cmp_lt_u32_e64 s[20:21], 6, v122
	v_cmp_lt_u32_e64 s[18:19], 7, v122
	v_cmp_lt_u32_e64 s[16:17], 8, v122
	v_cmp_lt_u32_e64 s[14:15], 9, v122
	v_cmp_lt_u32_e64 s[12:13], 10, v122
	v_cmp_lt_u32_e64 s[10:11], 11, v122
	v_cmp_lt_u32_e64 s[8:9], 12, v122
	v_cmp_lt_u32_e64 s[6:7], 13, v122
	v_cmp_eq_u32_e64 s[4:5], 15, v122
	v_pk_mul_f32 v[42:43], v[6:7], v[6:7]
	v_add_f32_e32 v12, v6, v6
	v_sub_f32_e32 v2, v42, v43
	v_mul_f32_e32 v12, v7, v12
	v_add_f32_e32 v42, v2, v2
	v_mul_f32_e32 v2, v2, v2
	v_mov_b32_e32 v108, v109
	v_fma_f32 v2, -v12, v12, v2
	v_mul_f32_e32 v12, v12, v42
	v_mov_b64_e32 v[42:43], v[108:109]
	s_and_saveexec_b64 s[72:73], s[30:31]
	s_cbranch_execnz .LBB1_119
	s_or_b64 exec, exec, s[72:73]
	s_and_saveexec_b64 s[30:31], s[28:29]
	s_cbranch_execnz .LBB1_124
